# speedup vs baseline: 1.0034x; 1.0034x over previous
.LBB3_11:
	s_lshl_b32 s58, s42, 7
	s_add_i32 s59, s41, 0x400
	s_lshr_b32 s59, s59, 6
	s_bfe_u32 s60, s20, 0x1000c
	s_add_i32 s59, s59, s60
	s_lshl_b32 s59, s59, 19
	s_add_u32 s58, s58, s59
	s_add_u32 s58, s56, s58
	s_addc_u32 s59, s57, 0
	s_add_u32 s60, s58, 0x4000
	s_addc_u32 s61, s59, 0
	s_add_u32 s62, s58, 0x100000
	s_addc_u32 s63, s59, 0
	s_add_u32 s64, s62, 0x4000
	s_addc_u32 s65, s63, 0
	s_lshr_b32 s66, s41, 7
	s_bfe_u32 s67, s20, 0x1000c
	s_add_i32 s66, s66, s67
	s_lshl_b32 s66, s66, 14
	s_lshl_b32 s67, s42, 2
	s_add_u32 s66, s66, s67
	s_add_u32 s66, s14, s66
	s_addc_u32 s67, s15, 0
	v_add_u32_e32 v172, s43, v207
	v_pk_fma_f32 v[244:245], v[244:245], -0.5, -0.5 op_sel_hi:[1,0,0]
	v_pk_fma_f32 v[246:247], v[246:247], -0.5, -0.5 op_sel_hi:[1,0,0]
	v_pk_fma_f32 v[248:249], v[248:249], -0.5, -0.5 op_sel_hi:[1,0,0]
	v_pk_fma_f32 v[250:251], v[250:251], -0.5, -0.5 op_sel_hi:[1,0,0]
	v_pk_fma_f32 v[252:253], v[252:253], -0.5, -0.5 op_sel_hi:[1,0,0]
	v_pk_fma_f32 v[254:255], v[254:255], -0.5, -0.5 op_sel_hi:[1,0,0]
	v_pk_fma_f32 v[232:233], v[232:233], -0.5, -0.5 op_sel_hi:[1,0,0]
	v_pk_fma_f32 v[234:235], v[234:235], -0.5, -0.5 op_sel_hi:[1,0,0]
	v_pk_mul_f32 v[134:135], v[244:245], v[246:247]
	v_pk_mul_f32 v[146:147], v[248:249], v[250:251]
	v_pk_mul_f32 v[180:181], v[252:253], v[254:255]
	v_pk_mul_f32 v[236:237], v[232:233], v[234:235]
	v_mul_f32_e32 v138, v134, v135
	v_mul_f32_e32 v150, v146, v147
	v_mul_f32_e32 v184, v180, v181
	v_mul_f32_e32 v240, v236, v237
	v_rcp_f32_e32 v138, v138
	v_rcp_f32_e32 v150, v150
	v_rcp_f32_e32 v184, v184
	v_rcp_f32_e32 v240, v240
	v_pk_add_f32 v[164:165], v[114:115], v[116:117]
	v_pk_add_f32 v[164:165], v[164:165], v[78:79]
	v_pk_add_f32 v[164:165], v[164:165], v[80:81]
	v_pk_add_f32 v[164:165], v[164:165], v[106:107]
	v_pk_add_f32 v[164:165], v[164:165], v[108:109]
	v_pk_add_f32 v[164:165], v[164:165], v[70:71]
	v_pk_add_f32 v[164:165], v[164:165], v[72:73]
	v_pk_mul_f32 v[162:163], v[134:135], v[146:147]
	v_pk_mul_f32 v[162:163], v[162:163], v[180:181]
	v_pk_mul_f32 v[162:163], v[162:163], v[236:237]
	v_pk_mul_f32 v[136:137], v[138:139], v[134:135] op_sel:[0,1] op_sel_hi:[0,0]
	v_pk_mul_f32 v[148:149], v[150:151], v[146:147] op_sel:[0,1] op_sel_hi:[0,0]
	v_pk_mul_f32 v[182:183], v[184:185], v[180:181] op_sel:[0,1] op_sel_hi:[0,0]
	v_pk_mul_f32 v[238:239], v[240:241], v[236:237] op_sel:[0,1] op_sel_hi:[0,0]
	v_pk_fma_f32 v[138:139], v[136:137], v[246:247], 1.0 op_sel_hi:[1,1,0]
	v_pk_fma_f32 v[140:141], v[136:137], v[244:245], 1.0 op_sel_hi:[1,1,0]
	v_pk_fma_f32 v[150:151], v[148:149], v[250:251], 1.0 op_sel_hi:[1,1,0]
	v_pk_fma_f32 v[152:153], v[148:149], v[248:249], 1.0 op_sel_hi:[1,1,0]
	v_pk_fma_f32 v[184:185], v[182:183], v[254:255], 1.0 op_sel_hi:[1,1,0]
	v_pk_fma_f32 v[186:187], v[182:183], v[252:253], 1.0 op_sel_hi:[1,1,0]
	v_pk_fma_f32 v[240:241], v[238:239], v[234:235], 1.0 op_sel_hi:[1,1,0]
	v_pk_fma_f32 v[242:243], v[238:239], v[232:233], 1.0 op_sel_hi:[1,1,0]
	v_cvt_pk_bf16_f32 v154, v138, v139
	v_cvt_pk_bf16_f32 v155, v140, v141
	v_cvt_pk_bf16_f32 v156, v150, v151
	v_cvt_pk_bf16_f32 v157, v152, v153
	v_cvt_pk_bf16_f32 v158, v184, v185
	v_cvt_pk_bf16_f32 v159, v186, v187
	v_cvt_pk_bf16_f32 v160, v240, v241
	v_cvt_pk_bf16_f32 v161, v242, v243
	ds_read_b128 v[114:117], v172
	ds_read_b128 v[78:81], v172 offset:64
	ds_read_b128 v[106:109], v172 offset:128
	ds_read_b128 v[70:73], v172 offset:192
	v_permlane16_swap_b32_e32 v154, v156
	v_permlane16_swap_b32_e32 v155, v157
	global_store_dwordx4 v228, v[154:157], s[58:59] nt
	v_permlane16_swap_b32_e32 v158, v160
	v_permlane16_swap_b32_e32 v159, v161
	global_store_dwordx4 v228, v[158:161], s[58:59] offset:128 nt
	v_exp_f32_e32 v130, v90
	v_exp_f32_e32 v131, v91
	v_exp_f32_e32 v132, v92
	v_exp_f32_e32 v133, v93
	v_exp_f32_e32 v142, v42
	v_exp_f32_e32 v143, v43
	v_exp_f32_e32 v144, v44
	v_exp_f32_e32 v145, v45
	v_exp_f32_e32 v176, v126
	v_exp_f32_e32 v177, v127
	v_exp_f32_e32 v178, v128
	v_exp_f32_e32 v179, v129
	v_exp_f32_e32 v232, v58
	v_exp_f32_e32 v233, v59
	v_exp_f32_e32 v234, v60
	v_exp_f32_e32 v235, v61
	s_bitcmp1_b32 s20, 12
	s_cbranch_scc1 .Lg1_noX
	s_barrier
.Lg1_noX:
	v_pk_fma_f32 v[130:131], v[130:131], -0.5, -0.5 op_sel_hi:[1,0,0]
	v_pk_fma_f32 v[132:133], v[132:133], -0.5, -0.5 op_sel_hi:[1,0,0]
	v_pk_fma_f32 v[142:143], v[142:143], -0.5, -0.5 op_sel_hi:[1,0,0]
	v_pk_fma_f32 v[144:145], v[144:145], -0.5, -0.5 op_sel_hi:[1,0,0]
	v_pk_fma_f32 v[176:177], v[176:177], -0.5, -0.5 op_sel_hi:[1,0,0]
	v_pk_fma_f32 v[178:179], v[178:179], -0.5, -0.5 op_sel_hi:[1,0,0]
	v_pk_fma_f32 v[232:233], v[232:233], -0.5, -0.5 op_sel_hi:[1,0,0]
	v_pk_fma_f32 v[234:235], v[234:235], -0.5, -0.5 op_sel_hi:[1,0,0]
	v_pk_mul_f32 v[134:135], v[130:131], v[132:133]
	v_pk_mul_f32 v[146:147], v[142:143], v[144:145]
	v_pk_mul_f32 v[180:181], v[176:177], v[178:179]
	v_pk_mul_f32 v[236:237], v[232:233], v[234:235]
	v_mul_f32_e32 v138, v134, v135
	v_mul_f32_e32 v150, v146, v147
	v_mul_f32_e32 v184, v180, v181
	v_mul_f32_e32 v240, v236, v237
	v_rcp_f32_e32 v138, v138
	v_rcp_f32_e32 v150, v150
	v_rcp_f32_e32 v184, v184
	v_rcp_f32_e32 v240, v240
	v_pk_add_f32 v[164:165], v[164:165], v[90:91]
	v_pk_add_f32 v[164:165], v[164:165], v[92:93]
	v_pk_add_f32 v[164:165], v[164:165], v[42:43]
	v_pk_add_f32 v[164:165], v[164:165], v[44:45]
	v_pk_add_f32 v[164:165], v[164:165], v[126:127]
	v_pk_add_f32 v[164:165], v[164:165], v[128:129]
	v_pk_add_f32 v[164:165], v[164:165], v[58:59]
	v_pk_add_f32 v[164:165], v[164:165], v[60:61]
	v_pk_mul_f32 v[174:175], v[134:135], v[146:147]
	v_pk_mul_f32 v[174:175], v[174:175], v[180:181]
	v_pk_mul_f32 v[174:175], v[174:175], v[236:237]
	v_pk_mul_f32 v[136:137], v[138:139], v[134:135] op_sel:[0,1] op_sel_hi:[0,0]
	v_pk_mul_f32 v[148:149], v[150:151], v[146:147] op_sel:[0,1] op_sel_hi:[0,0]
	v_pk_mul_f32 v[182:183], v[184:185], v[180:181] op_sel:[0,1] op_sel_hi:[0,0]
	v_pk_mul_f32 v[238:239], v[240:241], v[236:237] op_sel:[0,1] op_sel_hi:[0,0]
	v_pk_fma_f32 v[138:139], v[136:137], v[132:133], 1.0 op_sel_hi:[1,1,0]
	v_pk_fma_f32 v[140:141], v[136:137], v[130:131], 1.0 op_sel_hi:[1,1,0]
	v_pk_fma_f32 v[150:151], v[148:149], v[144:145], 1.0 op_sel_hi:[1,1,0]
	v_pk_fma_f32 v[152:153], v[148:149], v[142:143], 1.0 op_sel_hi:[1,1,0]
	v_pk_fma_f32 v[184:185], v[182:183], v[178:179], 1.0 op_sel_hi:[1,1,0]
	v_pk_fma_f32 v[186:187], v[182:183], v[176:177], 1.0 op_sel_hi:[1,1,0]
	v_pk_fma_f32 v[240:241], v[238:239], v[234:235], 1.0 op_sel_hi:[1,1,0]
	v_pk_fma_f32 v[242:243], v[238:239], v[232:233], 1.0 op_sel_hi:[1,1,0]
	v_cvt_pk_bf16_f32 v154, v138, v139
	v_cvt_pk_bf16_f32 v155, v140, v141
	v_cvt_pk_bf16_f32 v156, v150, v151
	v_cvt_pk_bf16_f32 v157, v152, v153
	v_cvt_pk_bf16_f32 v158, v184, v185
	v_cvt_pk_bf16_f32 v159, v186, v187
	v_cvt_pk_bf16_f32 v160, v240, v241
	v_cvt_pk_bf16_f32 v161, v242, v243
	ds_read_b128 v[90:93], v172 offset:512
	ds_read_b128 v[42:45], v172 offset:576
	ds_read_b128 v[126:129], v172 offset:640
	ds_read_b128 v[58:61], v172 offset:704
	v_permlane16_swap_b32_e32 v154, v156
	v_permlane16_swap_b32_e32 v155, v157
	global_store_dwordx4 v228, v[154:157], s[62:63] nt
	v_permlane16_swap_b32_e32 v158, v160
	v_permlane16_swap_b32_e32 v159, v161
	global_store_dwordx4 v228, v[158:161], s[62:63] offset:128 nt
	v_log_f32_e32 v166, v162
	v_log_f32_e32 v167, v163
	v_log_f32_e32 v170, v174
	v_log_f32_e32 v171, v175
	v_add_f32_e32 v168, v164, v165
	v_mul_f32_e32 v168, 0xbeb17218, v168
	v_add_f32_e32 v166, v166, v167
	v_add_f32_e32 v170, v170, v171
	v_add_f32_e32 v166, v166, v170
	v_fmac_f32_e32 v168, 0x3f317218, v166
	v_mov_b32_e32 v169, v168
	s_nop 1
	v_permlane16_swap_b32_e32 v168, v169
	v_add_f32_e32 v168, v168, v169
	v_mov_b32_e32 v169, v168
	s_nop 1
	v_permlane32_swap_b32_e32 v168, v169
	v_add_f32_e32 v168, v168, v169
	s_mov_b64 exec, s[0:1]
	global_store_dword v229, v168, s[66:67]
	s_mov_b64 exec, -1
	v_exp_f32_e32 v130, v110
	v_exp_f32_e32 v131, v111
	v_exp_f32_e32 v132, v112
	v_exp_f32_e32 v133, v113
	v_exp_f32_e32 v142, v74
	v_exp_f32_e32 v143, v75
	v_exp_f32_e32 v144, v76
	v_exp_f32_e32 v145, v77
	v_exp_f32_e32 v176, v102
	v_exp_f32_e32 v177, v103
	v_exp_f32_e32 v178, v104
	v_exp_f32_e32 v179, v105
	v_exp_f32_e32 v232, v66
	v_exp_f32_e32 v233, v67
	v_exp_f32_e32 v234, v68
	v_exp_f32_e32 v235, v69
	v_pk_fma_f32 v[130:131], v[130:131], -0.5, -0.5 op_sel_hi:[1,0,0]
	v_pk_fma_f32 v[132:133], v[132:133], -0.5, -0.5 op_sel_hi:[1,0,0]
	v_pk_fma_f32 v[142:143], v[142:143], -0.5, -0.5 op_sel_hi:[1,0,0]
	v_pk_fma_f32 v[144:145], v[144:145], -0.5, -0.5 op_sel_hi:[1,0,0]
	v_pk_fma_f32 v[176:177], v[176:177], -0.5, -0.5 op_sel_hi:[1,0,0]
	v_pk_fma_f32 v[178:179], v[178:179], -0.5, -0.5 op_sel_hi:[1,0,0]
	v_pk_fma_f32 v[232:233], v[232:233], -0.5, -0.5 op_sel_hi:[1,0,0]
	v_pk_fma_f32 v[234:235], v[234:235], -0.5, -0.5 op_sel_hi:[1,0,0]
	v_pk_mul_f32 v[134:135], v[130:131], v[132:133]
	v_pk_mul_f32 v[146:147], v[142:143], v[144:145]
	v_pk_mul_f32 v[180:181], v[176:177], v[178:179]
	v_pk_mul_f32 v[236:237], v[232:233], v[234:235]
	v_mul_f32_e32 v138, v134, v135
	v_mul_f32_e32 v150, v146, v147
	v_mul_f32_e32 v184, v180, v181
	v_mul_f32_e32 v240, v236, v237
	v_rcp_f32_e32 v138, v138
	v_rcp_f32_e32 v150, v150
	v_rcp_f32_e32 v184, v184
	v_rcp_f32_e32 v240, v240
	v_pk_add_f32 v[164:165], v[110:111], v[112:113]
	v_pk_add_f32 v[164:165], v[164:165], v[74:75]
	v_pk_add_f32 v[164:165], v[164:165], v[76:77]
	v_pk_add_f32 v[164:165], v[164:165], v[102:103]
	v_pk_add_f32 v[164:165], v[164:165], v[104:105]
	v_pk_add_f32 v[164:165], v[164:165], v[66:67]
	v_pk_add_f32 v[164:165], v[164:165], v[68:69]
	v_pk_mul_f32 v[162:163], v[134:135], v[146:147]
	v_pk_mul_f32 v[162:163], v[162:163], v[180:181]
	v_pk_mul_f32 v[162:163], v[162:163], v[236:237]
	v_pk_mul_f32 v[136:137], v[138:139], v[134:135] op_sel:[0,1] op_sel_hi:[0,0]
	v_pk_mul_f32 v[148:149], v[150:151], v[146:147] op_sel:[0,1] op_sel_hi:[0,0]
	v_pk_mul_f32 v[182:183], v[184:185], v[180:181] op_sel:[0,1] op_sel_hi:[0,0]
	v_pk_mul_f32 v[238:239], v[240:241], v[236:237] op_sel:[0,1] op_sel_hi:[0,0]
	v_pk_fma_f32 v[138:139], v[136:137], v[132:133], 1.0 op_sel_hi:[1,1,0]
	v_pk_fma_f32 v[140:141], v[136:137], v[130:131], 1.0 op_sel_hi:[1,1,0]
	v_pk_fma_f32 v[150:151], v[148:149], v[144:145], 1.0 op_sel_hi:[1,1,0]
	v_pk_fma_f32 v[152:153], v[148:149], v[142:143], 1.0 op_sel_hi:[1,1,0]
	v_pk_fma_f32 v[184:185], v[182:183], v[178:179], 1.0 op_sel_hi:[1,1,0]
	v_pk_fma_f32 v[186:187], v[182:183], v[176:177], 1.0 op_sel_hi:[1,1,0]
	v_pk_fma_f32 v[240:241], v[238:239], v[234:235], 1.0 op_sel_hi:[1,1,0]
	v_pk_fma_f32 v[242:243], v[238:239], v[232:233], 1.0 op_sel_hi:[1,1,0]
	v_cvt_pk_bf16_f32 v154, v138, v139
	v_cvt_pk_bf16_f32 v155, v140, v141
	v_cvt_pk_bf16_f32 v156, v150, v151
	v_cvt_pk_bf16_f32 v157, v152, v153
	v_cvt_pk_bf16_f32 v158, v184, v185
	v_cvt_pk_bf16_f32 v159, v186, v187
	v_cvt_pk_bf16_f32 v160, v240, v241
	v_cvt_pk_bf16_f32 v161, v242, v243
	ds_read_b128 v[110:113], v172
	ds_read_b128 v[74:77], v172 offset:64
	ds_read_b128 v[102:105], v172 offset:128
	ds_read_b128 v[66:69], v172 offset:192
	v_permlane16_swap_b32_e32 v154, v156
	v_permlane16_swap_b32_e32 v155, v157
	global_store_dwordx4 v228, v[154:157], s[58:59] offset:2048 nt
	v_permlane16_swap_b32_e32 v158, v160
	v_permlane16_swap_b32_e32 v159, v161
	global_store_dwordx4 v228, v[158:161], s[58:59] offset:2176 nt
	v_exp_f32_e32 v130, v86
	v_exp_f32_e32 v131, v87
	v_exp_f32_e32 v132, v88
	v_exp_f32_e32 v133, v89
	v_exp_f32_e32 v142, v38
	v_exp_f32_e32 v143, v39
	v_exp_f32_e32 v144, v40
	v_exp_f32_e32 v145, v41
	v_exp_f32_e32 v176, v122
	v_exp_f32_e32 v177, v123
	v_exp_f32_e32 v178, v124
	v_exp_f32_e32 v179, v125
	v_exp_f32_e32 v232, v50
	v_exp_f32_e32 v233, v51
	v_exp_f32_e32 v234, v52
	v_exp_f32_e32 v235, v53
	v_pk_fma_f32 v[130:131], v[130:131], -0.5, -0.5 op_sel_hi:[1,0,0]
	v_pk_fma_f32 v[132:133], v[132:133], -0.5, -0.5 op_sel_hi:[1,0,0]
	v_pk_fma_f32 v[142:143], v[142:143], -0.5, -0.5 op_sel_hi:[1,0,0]
	v_pk_fma_f32 v[144:145], v[144:145], -0.5, -0.5 op_sel_hi:[1,0,0]
	v_pk_fma_f32 v[176:177], v[176:177], -0.5, -0.5 op_sel_hi:[1,0,0]
	v_pk_fma_f32 v[178:179], v[178:179], -0.5, -0.5 op_sel_hi:[1,0,0]
	v_pk_fma_f32 v[232:233], v[232:233], -0.5, -0.5 op_sel_hi:[1,0,0]
	v_pk_fma_f32 v[234:235], v[234:235], -0.5, -0.5 op_sel_hi:[1,0,0]
	v_pk_mul_f32 v[134:135], v[130:131], v[132:133]
	v_pk_mul_f32 v[146:147], v[142:143], v[144:145]
	v_pk_mul_f32 v[180:181], v[176:177], v[178:179]
	v_pk_mul_f32 v[236:237], v[232:233], v[234:235]
	v_mul_f32_e32 v138, v134, v135
	v_mul_f32_e32 v150, v146, v147
	v_mul_f32_e32 v184, v180, v181
	v_mul_f32_e32 v240, v236, v237
	v_rcp_f32_e32 v138, v138
	v_rcp_f32_e32 v150, v150
	v_rcp_f32_e32 v184, v184
	v_rcp_f32_e32 v240, v240
	v_pk_add_f32 v[164:165], v[164:165], v[86:87]
	v_pk_add_f32 v[164:165], v[164:165], v[88:89]
	v_pk_add_f32 v[164:165], v[164:165], v[38:39]
	v_pk_add_f32 v[164:165], v[164:165], v[40:41]
	v_pk_add_f32 v[164:165], v[164:165], v[122:123]
	v_pk_add_f32 v[164:165], v[164:165], v[124:125]
	v_pk_add_f32 v[164:165], v[164:165], v[50:51]
	v_pk_add_f32 v[164:165], v[164:165], v[52:53]
	v_pk_mul_f32 v[174:175], v[134:135], v[146:147]
	v_pk_mul_f32 v[174:175], v[174:175], v[180:181]
	v_pk_mul_f32 v[174:175], v[174:175], v[236:237]
	v_pk_mul_f32 v[136:137], v[138:139], v[134:135] op_sel:[0,1] op_sel_hi:[0,0]
	v_pk_mul_f32 v[148:149], v[150:151], v[146:147] op_sel:[0,1] op_sel_hi:[0,0]
	v_pk_mul_f32 v[182:183], v[184:185], v[180:181] op_sel:[0,1] op_sel_hi:[0,0]
	v_pk_mul_f32 v[238:239], v[240:241], v[236:237] op_sel:[0,1] op_sel_hi:[0,0]
	v_pk_fma_f32 v[138:139], v[136:137], v[132:133], 1.0 op_sel_hi:[1,1,0]
	v_pk_fma_f32 v[140:141], v[136:137], v[130:131], 1.0 op_sel_hi:[1,1,0]
	v_pk_fma_f32 v[150:151], v[148:149], v[144:145], 1.0 op_sel_hi:[1,1,0]
	v_pk_fma_f32 v[152:153], v[148:149], v[142:143], 1.0 op_sel_hi:[1,1,0]
	v_pk_fma_f32 v[184:185], v[182:183], v[178:179], 1.0 op_sel_hi:[1,1,0]
	v_pk_fma_f32 v[186:187], v[182:183], v[176:177], 1.0 op_sel_hi:[1,1,0]
	v_pk_fma_f32 v[240:241], v[238:239], v[234:235], 1.0 op_sel_hi:[1,1,0]
	v_pk_fma_f32 v[242:243], v[238:239], v[232:233], 1.0 op_sel_hi:[1,1,0]
	v_cvt_pk_bf16_f32 v154, v138, v139
	v_cvt_pk_bf16_f32 v155, v140, v141
	v_cvt_pk_bf16_f32 v156, v150, v151
	v_cvt_pk_bf16_f32 v157, v152, v153
	v_cvt_pk_bf16_f32 v158, v184, v185
	v_cvt_pk_bf16_f32 v159, v186, v187
	v_cvt_pk_bf16_f32 v160, v240, v241
	v_cvt_pk_bf16_f32 v161, v242, v243
	ds_read_b128 v[86:89], v172 offset:512
	ds_read_b128 v[38:41], v172 offset:576
	ds_read_b128 v[122:125], v172 offset:640
	ds_read_b128 v[50:53], v172 offset:704
	v_permlane16_swap_b32_e32 v154, v156
	v_permlane16_swap_b32_e32 v155, v157
	global_store_dwordx4 v228, v[154:157], s[62:63] offset:2048 nt
	v_permlane16_swap_b32_e32 v158, v160
	v_permlane16_swap_b32_e32 v159, v161
	global_store_dwordx4 v228, v[158:161], s[62:63] offset:2176 nt
	v_log_f32_e32 v166, v162
	v_log_f32_e32 v167, v163
	v_log_f32_e32 v170, v174
	v_log_f32_e32 v171, v175
	v_add_f32_e32 v168, v164, v165
	v_mul_f32_e32 v168, 0xbeb17218, v168
	v_add_f32_e32 v166, v166, v167
	v_add_f32_e32 v170, v170, v171
	v_add_f32_e32 v166, v166, v170
	v_fmac_f32_e32 v168, 0x3f317218, v166
	v_mov_b32_e32 v169, v168
	s_nop 1
	v_permlane16_swap_b32_e32 v168, v169
	v_add_f32_e32 v168, v168, v169
	v_mov_b32_e32 v169, v168
	s_nop 1
	v_permlane32_swap_b32_e32 v168, v169
	v_add_f32_e32 v168, v168, v169
	s_mov_b64 exec, s[0:1]
	global_store_dword v229, v168, s[66:67] offset:64
	s_mov_b64 exec, -1
	v_exp_f32_e32 v130, v98
	v_exp_f32_e32 v131, v99
	v_exp_f32_e32 v132, v100
	v_exp_f32_e32 v133, v101
	v_exp_f32_e32 v142, v62
	v_exp_f32_e32 v143, v63
	v_exp_f32_e32 v144, v64
	v_exp_f32_e32 v145, v65
	v_exp_f32_e32 v176, v94
	v_exp_f32_e32 v177, v95
	v_exp_f32_e32 v178, v96
	v_exp_f32_e32 v179, v97
	v_exp_f32_e32 v232, v54
	v_exp_f32_e32 v233, v55
	v_exp_f32_e32 v234, v56
	v_exp_f32_e32 v235, v57
	v_pk_fma_f32 v[130:131], v[130:131], -0.5, -0.5 op_sel_hi:[1,0,0]
	v_pk_fma_f32 v[132:133], v[132:133], -0.5, -0.5 op_sel_hi:[1,0,0]
	v_pk_fma_f32 v[142:143], v[142:143], -0.5, -0.5 op_sel_hi:[1,0,0]
	v_pk_fma_f32 v[144:145], v[144:145], -0.5, -0.5 op_sel_hi:[1,0,0]
	v_pk_fma_f32 v[176:177], v[176:177], -0.5, -0.5 op_sel_hi:[1,0,0]
	v_pk_fma_f32 v[178:179], v[178:179], -0.5, -0.5 op_sel_hi:[1,0,0]
	v_pk_fma_f32 v[232:233], v[232:233], -0.5, -0.5 op_sel_hi:[1,0,0]
	v_pk_fma_f32 v[234:235], v[234:235], -0.5, -0.5 op_sel_hi:[1,0,0]
	v_pk_mul_f32 v[134:135], v[130:131], v[132:133]
	v_pk_mul_f32 v[146:147], v[142:143], v[144:145]
	v_pk_mul_f32 v[180:181], v[176:177], v[178:179]
	v_pk_mul_f32 v[236:237], v[232:233], v[234:235]
	v_mul_f32_e32 v138, v134, v135
	v_mul_f32_e32 v150, v146, v147
	v_mul_f32_e32 v184, v180, v181
	v_mul_f32_e32 v240, v236, v237
	v_rcp_f32_e32 v138, v138
	v_rcp_f32_e32 v150, v150
	v_rcp_f32_e32 v184, v184
	v_rcp_f32_e32 v240, v240
	v_pk_add_f32 v[164:165], v[98:99], v[100:101]
	v_pk_add_f32 v[164:165], v[164:165], v[62:63]
	v_pk_add_f32 v[164:165], v[164:165], v[64:65]
	v_pk_add_f32 v[164:165], v[164:165], v[94:95]
	v_pk_add_f32 v[164:165], v[164:165], v[96:97]
	v_pk_add_f32 v[164:165], v[164:165], v[54:55]
	v_pk_add_f32 v[164:165], v[164:165], v[56:57]
	v_pk_mul_f32 v[162:163], v[134:135], v[146:147]
	v_pk_mul_f32 v[162:163], v[162:163], v[180:181]
	v_pk_mul_f32 v[162:163], v[162:163], v[236:237]
	v_pk_mul_f32 v[136:137], v[138:139], v[134:135] op_sel:[0,1] op_sel_hi:[0,0]
	v_pk_mul_f32 v[148:149], v[150:151], v[146:147] op_sel:[0,1] op_sel_hi:[0,0]
	v_pk_mul_f32 v[182:183], v[184:185], v[180:181] op_sel:[0,1] op_sel_hi:[0,0]
	v_pk_mul_f32 v[238:239], v[240:241], v[236:237] op_sel:[0,1] op_sel_hi:[0,0]
	v_pk_fma_f32 v[138:139], v[136:137], v[132:133], 1.0 op_sel_hi:[1,1,0]
	v_pk_fma_f32 v[140:141], v[136:137], v[130:131], 1.0 op_sel_hi:[1,1,0]
	v_pk_fma_f32 v[150:151], v[148:149], v[144:145], 1.0 op_sel_hi:[1,1,0]
	v_pk_fma_f32 v[152:153], v[148:149], v[142:143], 1.0 op_sel_hi:[1,1,0]
	v_pk_fma_f32 v[184:185], v[182:183], v[178:179], 1.0 op_sel_hi:[1,1,0]
	v_pk_fma_f32 v[186:187], v[182:183], v[176:177], 1.0 op_sel_hi:[1,1,0]
	v_pk_fma_f32 v[240:241], v[238:239], v[234:235], 1.0 op_sel_hi:[1,1,0]
	v_pk_fma_f32 v[242:243], v[238:239], v[232:233], 1.0 op_sel_hi:[1,1,0]
	v_cvt_pk_bf16_f32 v154, v138, v139
	v_cvt_pk_bf16_f32 v155, v140, v141
	v_cvt_pk_bf16_f32 v156, v150, v151
	v_cvt_pk_bf16_f32 v157, v152, v153
	v_cvt_pk_bf16_f32 v158, v184, v185
	v_cvt_pk_bf16_f32 v159, v186, v187
	v_cvt_pk_bf16_f32 v160, v240, v241
	v_cvt_pk_bf16_f32 v161, v242, v243
	ds_read_b128 v[98:101], v172
	ds_read_b128 v[62:65], v172 offset:64
	ds_read_b128 v[94:97], v172 offset:128
	ds_read_b128 v[54:57], v172 offset:192
	v_permlane16_swap_b32_e32 v154, v156
	v_permlane16_swap_b32_e32 v155, v157
	global_store_dwordx4 v228, v[154:157], s[60:61] nt
	v_permlane16_swap_b32_e32 v158, v160
	v_permlane16_swap_b32_e32 v159, v161
	global_store_dwordx4 v228, v[158:161], s[60:61] offset:128 nt
	v_exp_f32_e32 v130, v82
	v_exp_f32_e32 v131, v83
	v_exp_f32_e32 v132, v84
	v_exp_f32_e32 v133, v85
	v_exp_f32_e32 v142, v34
	v_exp_f32_e32 v143, v35
	v_exp_f32_e32 v144, v36
	v_exp_f32_e32 v145, v37
	v_exp_f32_e32 v176, v118
	v_exp_f32_e32 v177, v119
	v_exp_f32_e32 v178, v120
	v_exp_f32_e32 v179, v121
	v_exp_f32_e32 v232, v46
	v_exp_f32_e32 v233, v47
	v_exp_f32_e32 v234, v48
	v_exp_f32_e32 v235, v49
	v_pk_fma_f32 v[130:131], v[130:131], -0.5, -0.5 op_sel_hi:[1,0,0]
	v_pk_fma_f32 v[132:133], v[132:133], -0.5, -0.5 op_sel_hi:[1,0,0]
	v_pk_fma_f32 v[142:143], v[142:143], -0.5, -0.5 op_sel_hi:[1,0,0]
	v_pk_fma_f32 v[144:145], v[144:145], -0.5, -0.5 op_sel_hi:[1,0,0]
	v_pk_fma_f32 v[176:177], v[176:177], -0.5, -0.5 op_sel_hi:[1,0,0]
	v_pk_fma_f32 v[178:179], v[178:179], -0.5, -0.5 op_sel_hi:[1,0,0]
	v_pk_fma_f32 v[232:233], v[232:233], -0.5, -0.5 op_sel_hi:[1,0,0]
	v_pk_fma_f32 v[234:235], v[234:235], -0.5, -0.5 op_sel_hi:[1,0,0]
	v_pk_mul_f32 v[134:135], v[130:131], v[132:133]
	v_pk_mul_f32 v[146:147], v[142:143], v[144:145]
	v_pk_mul_f32 v[180:181], v[176:177], v[178:179]
	v_pk_mul_f32 v[236:237], v[232:233], v[234:235]
	v_mul_f32_e32 v138, v134, v135
	v_mul_f32_e32 v150, v146, v147
	v_mul_f32_e32 v184, v180, v181
	v_mul_f32_e32 v240, v236, v237
	v_rcp_f32_e32 v138, v138
	v_rcp_f32_e32 v150, v150
	v_rcp_f32_e32 v184, v184
	v_rcp_f32_e32 v240, v240
	v_pk_add_f32 v[164:165], v[164:165], v[82:83]
	v_pk_add_f32 v[164:165], v[164:165], v[84:85]
	v_pk_add_f32 v[164:165], v[164:165], v[34:35]
	v_pk_add_f32 v[164:165], v[164:165], v[36:37]
	v_pk_add_f32 v[164:165], v[164:165], v[118:119]
	v_pk_add_f32 v[164:165], v[164:165], v[120:121]
	v_pk_add_f32 v[164:165], v[164:165], v[46:47]
	v_pk_add_f32 v[164:165], v[164:165], v[48:49]
	v_pk_mul_f32 v[174:175], v[134:135], v[146:147]
	v_pk_mul_f32 v[174:175], v[174:175], v[180:181]
	v_pk_mul_f32 v[174:175], v[174:175], v[236:237]
	v_pk_mul_f32 v[136:137], v[138:139], v[134:135] op_sel:[0,1] op_sel_hi:[0,0]
	v_pk_mul_f32 v[148:149], v[150:151], v[146:147] op_sel:[0,1] op_sel_hi:[0,0]
	v_pk_mul_f32 v[182:183], v[184:185], v[180:181] op_sel:[0,1] op_sel_hi:[0,0]
	v_pk_mul_f32 v[238:239], v[240:241], v[236:237] op_sel:[0,1] op_sel_hi:[0,0]
	v_pk_fma_f32 v[138:139], v[136:137], v[132:133], 1.0 op_sel_hi:[1,1,0]
	v_pk_fma_f32 v[140:141], v[136:137], v[130:131], 1.0 op_sel_hi:[1,1,0]
	v_pk_fma_f32 v[150:151], v[148:149], v[144:145], 1.0 op_sel_hi:[1,1,0]
	v_pk_fma_f32 v[152:153], v[148:149], v[142:143], 1.0 op_sel_hi:[1,1,0]
	v_pk_fma_f32 v[184:185], v[182:183], v[178:179], 1.0 op_sel_hi:[1,1,0]
	v_pk_fma_f32 v[186:187], v[182:183], v[176:177], 1.0 op_sel_hi:[1,1,0]
	v_pk_fma_f32 v[240:241], v[238:239], v[234:235], 1.0 op_sel_hi:[1,1,0]
	v_pk_fma_f32 v[242:243], v[238:239], v[232:233], 1.0 op_sel_hi:[1,1,0]
	v_cvt_pk_bf16_f32 v154, v138, v139
	v_cvt_pk_bf16_f32 v155, v140, v141
	v_cvt_pk_bf16_f32 v156, v150, v151
	v_cvt_pk_bf16_f32 v157, v152, v153
	v_cvt_pk_bf16_f32 v158, v184, v185
	v_cvt_pk_bf16_f32 v159, v186, v187
	v_cvt_pk_bf16_f32 v160, v240, v241
	v_cvt_pk_bf16_f32 v161, v242, v243
	ds_read_b128 v[82:85], v172 offset:512
	ds_read_b128 v[34:37], v172 offset:576
	ds_read_b128 v[118:121], v172 offset:640
	ds_read_b128 v[46:49], v172 offset:704
	v_permlane16_swap_b32_e32 v154, v156
	v_permlane16_swap_b32_e32 v155, v157
	global_store_dwordx4 v228, v[154:157], s[64:65] nt
	v_permlane16_swap_b32_e32 v158, v160
	v_permlane16_swap_b32_e32 v159, v161
	global_store_dwordx4 v228, v[158:161], s[64:65] offset:128 nt
	v_log_f32_e32 v166, v162
	v_log_f32_e32 v167, v163
	v_log_f32_e32 v170, v174
	v_log_f32_e32 v171, v175
	v_add_f32_e32 v168, v164, v165
	v_mul_f32_e32 v168, 0xbeb17218, v168
	v_add_f32_e32 v166, v166, v167
	v_add_f32_e32 v170, v170, v171
	v_add_f32_e32 v166, v166, v170
	v_fmac_f32_e32 v168, 0x3f317218, v166
	v_mov_b32_e32 v169, v168
	s_nop 1
	v_permlane16_swap_b32_e32 v168, v169
	v_add_f32_e32 v168, v168, v169
	v_mov_b32_e32 v169, v168
	s_nop 1
	v_permlane32_swap_b32_e32 v168, v169
	v_add_f32_e32 v168, v168, v169
	s_mov_b64 exec, s[0:1]
	global_store_dword v229, v168, s[66:67] offset:512
	s_mov_b64 exec, -1
	v_exp_f32_e32 v130, v18
	v_exp_f32_e32 v131, v19
	v_exp_f32_e32 v132, v20
	v_exp_f32_e32 v133, v21
	v_exp_f32_e32 v142, v2
	v_exp_f32_e32 v143, v3
	v_exp_f32_e32 v144, v4
	v_exp_f32_e32 v145, v5
	v_exp_f32_e32 v176, v26
	v_exp_f32_e32 v177, v27
	v_exp_f32_e32 v178, v28
	v_exp_f32_e32 v179, v29
	v_exp_f32_e32 v232, v10
	v_exp_f32_e32 v233, v11
	v_exp_f32_e32 v234, v12
	v_exp_f32_e32 v235, v13
	v_pk_fma_f32 v[130:131], v[130:131], -0.5, -0.5 op_sel_hi:[1,0,0]
	v_pk_fma_f32 v[132:133], v[132:133], -0.5, -0.5 op_sel_hi:[1,0,0]
	v_pk_fma_f32 v[142:143], v[142:143], -0.5, -0.5 op_sel_hi:[1,0,0]
	v_pk_fma_f32 v[144:145], v[144:145], -0.5, -0.5 op_sel_hi:[1,0,0]
	v_pk_fma_f32 v[176:177], v[176:177], -0.5, -0.5 op_sel_hi:[1,0,0]
	v_pk_fma_f32 v[178:179], v[178:179], -0.5, -0.5 op_sel_hi:[1,0,0]
	v_pk_fma_f32 v[232:233], v[232:233], -0.5, -0.5 op_sel_hi:[1,0,0]
	v_pk_fma_f32 v[234:235], v[234:235], -0.5, -0.5 op_sel_hi:[1,0,0]
	v_pk_mul_f32 v[134:135], v[130:131], v[132:133]
	v_pk_mul_f32 v[146:147], v[142:143], v[144:145]
	v_pk_mul_f32 v[180:181], v[176:177], v[178:179]
	v_pk_mul_f32 v[236:237], v[232:233], v[234:235]
	v_mul_f32_e32 v138, v134, v135
	v_mul_f32_e32 v150, v146, v147
	v_mul_f32_e32 v184, v180, v181
	v_mul_f32_e32 v240, v236, v237
	v_rcp_f32_e32 v138, v138
	v_rcp_f32_e32 v150, v150
	v_rcp_f32_e32 v184, v184
	v_rcp_f32_e32 v240, v240
	v_pk_add_f32 v[164:165], v[18:19], v[20:21]
	v_pk_add_f32 v[164:165], v[164:165], v[2:3]
	v_pk_add_f32 v[164:165], v[164:165], v[4:5]
	v_pk_add_f32 v[164:165], v[164:165], v[26:27]
	v_pk_add_f32 v[164:165], v[164:165], v[28:29]
	v_pk_add_f32 v[164:165], v[164:165], v[10:11]
	v_pk_add_f32 v[164:165], v[164:165], v[12:13]
	v_pk_mul_f32 v[162:163], v[134:135], v[146:147]
	v_pk_mul_f32 v[162:163], v[162:163], v[180:181]
	v_pk_mul_f32 v[162:163], v[162:163], v[236:237]
	v_pk_mul_f32 v[136:137], v[138:139], v[134:135] op_sel:[0,1] op_sel_hi:[0,0]
	v_pk_mul_f32 v[148:149], v[150:151], v[146:147] op_sel:[0,1] op_sel_hi:[0,0]
	v_pk_mul_f32 v[182:183], v[184:185], v[180:181] op_sel:[0,1] op_sel_hi:[0,0]
	v_pk_mul_f32 v[238:239], v[240:241], v[236:237] op_sel:[0,1] op_sel_hi:[0,0]
	v_pk_fma_f32 v[138:139], v[136:137], v[132:133], 1.0 op_sel_hi:[1,1,0]
	v_pk_fma_f32 v[140:141], v[136:137], v[130:131], 1.0 op_sel_hi:[1,1,0]
	v_pk_fma_f32 v[150:151], v[148:149], v[144:145], 1.0 op_sel_hi:[1,1,0]
	v_pk_fma_f32 v[152:153], v[148:149], v[142:143], 1.0 op_sel_hi:[1,1,0]
	v_pk_fma_f32 v[184:185], v[182:183], v[178:179], 1.0 op_sel_hi:[1,1,0]
	v_pk_fma_f32 v[186:187], v[182:183], v[176:177], 1.0 op_sel_hi:[1,1,0]
	v_pk_fma_f32 v[240:241], v[238:239], v[234:235], 1.0 op_sel_hi:[1,1,0]
	v_pk_fma_f32 v[242:243], v[238:239], v[232:233], 1.0 op_sel_hi:[1,1,0]
	v_cvt_pk_bf16_f32 v154, v138, v139
	v_cvt_pk_bf16_f32 v155, v140, v141
	v_cvt_pk_bf16_f32 v156, v150, v151
	v_cvt_pk_bf16_f32 v157, v152, v153
	v_cvt_pk_bf16_f32 v158, v184, v185
	v_cvt_pk_bf16_f32 v159, v186, v187
	v_cvt_pk_bf16_f32 v160, v240, v241
	v_cvt_pk_bf16_f32 v161, v242, v243
	ds_read_b128 v[18:21], v172
	ds_read_b128 v[2:5], v172 offset:64
	ds_read_b128 v[26:29], v172 offset:128
	ds_read_b128 v[10:13], v172 offset:192
	v_permlane16_swap_b32_e32 v154, v156
	v_permlane16_swap_b32_e32 v155, v157
	global_store_dwordx4 v228, v[154:157], s[60:61] offset:2048 nt
	v_permlane16_swap_b32_e32 v158, v160
	v_permlane16_swap_b32_e32 v159, v161
	global_store_dwordx4 v228, v[158:161], s[60:61] offset:2176 nt
	v_exp_f32_e32 v130, v22
	v_exp_f32_e32 v131, v23
	v_exp_f32_e32 v132, v24
	v_exp_f32_e32 v133, v25
	v_exp_f32_e32 v142, v6
	v_exp_f32_e32 v143, v7
	v_exp_f32_e32 v144, v8
	v_exp_f32_e32 v145, v9
	v_exp_f32_e32 v176, v30
	v_exp_f32_e32 v177, v31
	v_exp_f32_e32 v178, v32
	v_exp_f32_e32 v179, v33
	v_exp_f32_e32 v232, v14
	v_exp_f32_e32 v233, v15
	v_exp_f32_e32 v234, v16
	v_exp_f32_e32 v235, v17
	v_pk_fma_f32 v[130:131], v[130:131], -0.5, -0.5 op_sel_hi:[1,0,0]
	v_pk_fma_f32 v[132:133], v[132:133], -0.5, -0.5 op_sel_hi:[1,0,0]
	v_pk_fma_f32 v[142:143], v[142:143], -0.5, -0.5 op_sel_hi:[1,0,0]
	v_pk_fma_f32 v[144:145], v[144:145], -0.5, -0.5 op_sel_hi:[1,0,0]
	v_pk_fma_f32 v[176:177], v[176:177], -0.5, -0.5 op_sel_hi:[1,0,0]
	v_pk_fma_f32 v[178:179], v[178:179], -0.5, -0.5 op_sel_hi:[1,0,0]
	v_pk_fma_f32 v[232:233], v[232:233], -0.5, -0.5 op_sel_hi:[1,0,0]
	v_pk_fma_f32 v[234:235], v[234:235], -0.5, -0.5 op_sel_hi:[1,0,0]
	v_pk_mul_f32 v[134:135], v[130:131], v[132:133]
	v_pk_mul_f32 v[146:147], v[142:143], v[144:145]
	v_pk_mul_f32 v[180:181], v[176:177], v[178:179]
	v_pk_mul_f32 v[236:237], v[232:233], v[234:235]
	v_mul_f32_e32 v138, v134, v135
	v_mul_f32_e32 v150, v146, v147
	v_mul_f32_e32 v184, v180, v181
	v_mul_f32_e32 v240, v236, v237
	v_rcp_f32_e32 v138, v138
	v_rcp_f32_e32 v150, v150
	v_rcp_f32_e32 v184, v184
	v_rcp_f32_e32 v240, v240
	v_pk_add_f32 v[164:165], v[164:165], v[22:23]
	v_pk_add_f32 v[164:165], v[164:165], v[24:25]
	v_pk_add_f32 v[164:165], v[164:165], v[6:7]
	v_pk_add_f32 v[164:165], v[164:165], v[8:9]
	v_pk_add_f32 v[164:165], v[164:165], v[30:31]
	v_pk_add_f32 v[164:165], v[164:165], v[32:33]
	v_pk_add_f32 v[164:165], v[164:165], v[14:15]
	v_pk_add_f32 v[164:165], v[164:165], v[16:17]
	v_pk_mul_f32 v[174:175], v[134:135], v[146:147]
	v_pk_mul_f32 v[174:175], v[174:175], v[180:181]
	v_pk_mul_f32 v[174:175], v[174:175], v[236:237]
	v_pk_mul_f32 v[136:137], v[138:139], v[134:135] op_sel:[0,1] op_sel_hi:[0,0]
	v_pk_mul_f32 v[148:149], v[150:151], v[146:147] op_sel:[0,1] op_sel_hi:[0,0]
	v_pk_mul_f32 v[182:183], v[184:185], v[180:181] op_sel:[0,1] op_sel_hi:[0,0]
	v_pk_mul_f32 v[238:239], v[240:241], v[236:237] op_sel:[0,1] op_sel_hi:[0,0]
	v_pk_fma_f32 v[138:139], v[136:137], v[132:133], 1.0 op_sel_hi:[1,1,0]
	v_pk_fma_f32 v[140:141], v[136:137], v[130:131], 1.0 op_sel_hi:[1,1,0]
	v_pk_fma_f32 v[150:151], v[148:149], v[144:145], 1.0 op_sel_hi:[1,1,0]
	v_pk_fma_f32 v[152:153], v[148:149], v[142:143], 1.0 op_sel_hi:[1,1,0]
	v_pk_fma_f32 v[184:185], v[182:183], v[178:179], 1.0 op_sel_hi:[1,1,0]
	v_pk_fma_f32 v[186:187], v[182:183], v[176:177], 1.0 op_sel_hi:[1,1,0]
	v_pk_fma_f32 v[240:241], v[238:239], v[234:235], 1.0 op_sel_hi:[1,1,0]
	v_pk_fma_f32 v[242:243], v[238:239], v[232:233], 1.0 op_sel_hi:[1,1,0]
	v_cvt_pk_bf16_f32 v154, v138, v139
	v_cvt_pk_bf16_f32 v155, v140, v141
	v_cvt_pk_bf16_f32 v156, v150, v151
	v_cvt_pk_bf16_f32 v157, v152, v153
	v_cvt_pk_bf16_f32 v158, v184, v185
	v_cvt_pk_bf16_f32 v159, v186, v187
	v_cvt_pk_bf16_f32 v160, v240, v241
	v_cvt_pk_bf16_f32 v161, v242, v243
	ds_read_b128 v[22:25], v172 offset:512
	ds_read_b128 v[6:9], v172 offset:576
	ds_read_b128 v[30:33], v172 offset:640
	ds_read_b128 v[14:17], v172 offset:704
	v_permlane16_swap_b32_e32 v154, v156
	v_permlane16_swap_b32_e32 v155, v157
	global_store_dwordx4 v228, v[154:157], s[64:65] offset:2048 nt
	v_permlane16_swap_b32_e32 v158, v160
	v_permlane16_swap_b32_e32 v159, v161
	global_store_dwordx4 v228, v[158:161], s[64:65] offset:2176 nt
	v_log_f32_e32 v166, v162
	v_log_f32_e32 v167, v163
	v_log_f32_e32 v170, v174
	v_log_f32_e32 v171, v175
	v_add_f32_e32 v168, v164, v165
	v_mul_f32_e32 v168, 0xbeb17218, v168
	v_add_f32_e32 v166, v166, v167
	v_add_f32_e32 v170, v170, v171
	v_add_f32_e32 v166, v166, v170
	v_fmac_f32_e32 v168, 0x3f317218, v166
	v_mov_b32_e32 v169, v168
	s_nop 1
	v_permlane16_swap_b32_e32 v168, v169
	v_add_f32_e32 v168, v168, v169
	v_mov_b32_e32 v169, v168
	s_nop 1
	v_permlane32_swap_b32_e32 v168, v169
	v_add_f32_e32 v168, v168, v169
	s_mov_b64 exec, s[0:1]
	global_store_dword v229, v168, s[66:67] offset:576
	s_mov_b64 exec, -1
	s_bitcmp1_b32 s20, 12
	s_cbranch_scc0 .Lg1_noY
	s_barrier
